# speedup vs baseline: 1.0303x; 1.0303x over previous
.LBB3_4:
	s_or_b64 exec, exec, s[4:5]
	v_readfirstlane_b32 s34, v0
	s_lshr_b32 s51, s34, 7
	s_add_i32 s51, s51, s48
	s_lshl_b32 s4, s51, 6
	s_add_i32 s4, s4, s47
	s_lshl_b32 s5, s28, 1
	s_bfe_u32 s29, s34, 0x10006
	s_or_b32 s4, s4, s5
	s_or_b32 s4, s4, s29
	s_lshr_b32 s53, s34, 6
	s_lshl_b32 s4, s4, 11
	s_ashr_i32 s5, s4, 31
	s_lshl_b32 s16, s53, 10
	s_cmp_lg_u32 0, -1
	s_cselect_b32 s6, 0, 0
	v_or_b32_e32 v246, s16, v226
	s_add_i32 s56, s16, s6
	s_mov_b32 s6, m0
	s_mov_b32 m0, s56
	s_nop 0
	global_load_lds_dwordx4 v246, s[18:19]
	s_mov_b32 m0, s6
	s_add_i32 s57, s56, 0x6000
	s_mov_b32 s6, m0
	s_mov_b32 m0, s57
	s_nop 0
	global_load_lds_dwordx4 v246, s[8:9]
	s_mov_b32 m0, s6
	s_add_i32 s6, s56, 0x2000
	s_mov_b32 s7, m0
	s_mov_b32 m0, s6
	s_nop 0
	global_load_lds_dwordx4 v246, s[20:21]
	s_mov_b32 m0, s7
	v_lshl_add_u64 v[4:5], s[4:5], 1, v[222:223]
	global_load_dwordx4 v[162:165], v[4:5], off nt
	global_load_dwordx4 v[154:157], v[4:5], off offset:1024 nt
	global_load_dwordx4 v[150:153], v[4:5], off offset:2048 nt
	global_load_dwordx4 v[146:149], v[4:5], off offset:3072 nt
	v_mov_b64_e32 v[48:49], v[32:33]
	v_mov_b64_e32 v[46:47], v[30:31]
	v_mov_b64_e32 v[44:45], v[28:29]
	v_mov_b64_e32 v[42:43], v[26:27]
	v_mov_b64_e32 v[40:41], v[24:25]
	v_mov_b64_e32 v[38:39], v[22:23]
	v_mov_b64_e32 v[36:37], v[20:21]
	v_mov_b64_e32 v[34:35], v[18:19]
	s_add_i32 s4, s56, 0x4000
	s_mov_b32 s5, m0
	s_mov_b32 m0, s4
	s_nop 0
	global_load_lds_dwordx4 v246, s[22:23]
	s_mov_b32 m0, s5
	s_waitcnt vmcnt(3) lgkmcnt(0)
	s_barrier
	ds_read_b128 v[4:7], v230
	ds_read_b128 v[8:11], v230 offset:512
	s_lshl_b32 s54, s28, 6
	s_lshl_b32 s36, s29, 5
	s_or_b32 s52, s36, s54
	s_waitcnt vmcnt(3) lgkmcnt(1)
	v_mfma_f32_32x32x16_f16 v[50:65], v[4:7], v[162:165], v[34:49]
	s_waitcnt lgkmcnt(0)
	v_mfma_f32_32x32x16_f16 v[34:49], v[8:11], v[162:165], v[34:49]
	ds_read_b128 v[4:7], v230 offset:2048
	ds_read_b128 v[8:11], v230 offset:2560
	s_waitcnt vmcnt(2) lgkmcnt(1)
	v_mfma_f32_32x32x16_f16 v[50:65], v[4:7], v[154:157], v[50:65]
	s_waitcnt lgkmcnt(0)
	v_mfma_f32_32x32x16_f16 v[34:49], v[8:11], v[154:157], v[34:49]
	ds_read_b128 v[4:7], v230 offset:4096
	ds_read_b128 v[8:11], v230 offset:4608
	s_waitcnt vmcnt(1) lgkmcnt(1)
	v_mfma_f32_32x32x16_f16 v[50:65], v[4:7], v[150:153], v[50:65]
	s_waitcnt lgkmcnt(0)
	v_mfma_f32_32x32x16_f16 v[34:49], v[8:11], v[150:153], v[34:49]
	ds_read_b128 v[4:7], v230 offset:6144
	ds_read_b128 v[8:11], v230 offset:6656
	s_waitcnt vmcnt(0) lgkmcnt(1)
	v_mfma_f32_32x32x16_f16 v[50:65], v[4:7], v[146:149], v[50:65]
	v_and_b32_e32 v4, 1, v3
	v_bfe_u32 v3, v3, 1, 1
	v_cmp_ne_u32_e64 s[4:5], 0, v4
	v_cmp_ne_u32_e64 s[6:7], 0, v3
	v_or_b32_e32 v3, s52, v1
	v_lshlrev_b32_e32 v245, 8, v3
	s_bitcmp0_b32 s4, 0
	s_waitcnt lgkmcnt(0)
	v_mfma_f32_32x32x16_f16 v[34:49], v[8:11], v[146:149], v[34:49]
	s_nop 15
	s_nop 7
	s_cbranch_scc1 .LBB3_6
	global_load_dwordx2 v[4:5], v245, s[12:13]
	s_waitcnt vmcnt(0)
	v_lshrrev_b32_e32 v3, v231, v4
	v_bfe_u32 v4, v4, v231, 1
	v_lshrrev_b32_e32 v6, v231, v5
	v_bfe_u32 v5, v5, v231, 1
	v_cmp_eq_u32_e32 vcc, 0, v4
	v_and_b32_e32 v4, 2, v3
	v_and_b32_e32 v7, 4, v3
	v_cndmask_b32_e32 v50, v242, v50, vcc
	v_cmp_eq_u32_e32 vcc, 0, v5
	v_and_b32_e32 v5, 2, v6
	v_and_b32_e32 v8, 4, v6
	v_cndmask_b32_e32 v34, v242, v34, vcc
	v_cmp_eq_u32_e32 vcc, 0, v4
	v_and_b32_e32 v9, 8, v3
	v_and_b32_e32 v10, 8, v6
	v_cndmask_b32_e32 v51, v242, v51, vcc
	v_cmp_eq_u32_e32 vcc, 0, v5
	v_and_b32_e32 v11, 0x100, v3
	v_and_b32_e32 v12, 0x100, v6
	v_cndmask_b32_e32 v35, v242, v35, vcc
	v_cmp_eq_u32_e32 vcc, 0, v7
	v_and_b32_e32 v13, 0x200, v3
	v_and_b32_e32 v14, 0x200, v6
	v_cndmask_b32_e32 v52, v242, v52, vcc
	v_cmp_eq_u32_e32 vcc, 0, v8
	v_and_b32_e32 v15, 0x400, v3
	v_and_b32_e32 v16, 0x400, v6
	v_cndmask_b32_e32 v36, v242, v36, vcc
	v_cmp_eq_u32_e32 vcc, 0, v9
	v_and_b32_e32 v17, 0x800, v3
	v_and_b32_e32 v66, 0x800, v6
	v_cndmask_b32_e32 v53, v242, v53, vcc
	v_cmp_eq_u32_e32 vcc, 0, v10
	v_and_b32_e32 v67, 0x10000, v3
	v_and_b32_e32 v68, 0x10000, v6
	v_cndmask_b32_e32 v37, v242, v37, vcc
	v_cmp_eq_u32_e32 vcc, 0, v11
	v_and_b32_e32 v69, 0x20000, v3
	v_and_b32_e32 v70, 0x20000, v6
	v_cndmask_b32_e32 v54, v242, v54, vcc
	v_cmp_eq_u32_e32 vcc, 0, v12
	v_and_b32_e32 v71, 0x40000, v3
	v_and_b32_e32 v72, 0x40000, v6
	v_cndmask_b32_e32 v38, v242, v38, vcc
	v_cmp_eq_u32_e32 vcc, 0, v13
	v_and_b32_e32 v73, 0x80000, v3
	v_and_b32_e32 v74, 0x80000, v6
	v_cndmask_b32_e32 v55, v242, v55, vcc
	v_cmp_eq_u32_e32 vcc, 0, v14
	v_and_b32_e32 v75, 0x1000000, v3
	v_and_b32_e32 v76, 0x1000000, v6
	v_cndmask_b32_e32 v39, v242, v39, vcc
	v_cmp_eq_u32_e32 vcc, 0, v15
	v_and_b32_e32 v77, 0x2000000, v3
	v_and_b32_e32 v4, 0x2000000, v6
	v_cndmask_b32_e32 v56, v242, v56, vcc
	v_cmp_eq_u32_e32 vcc, 0, v16
	s_nop 1
	v_cndmask_b32_e32 v40, v242, v40, vcc
	v_cmp_eq_u32_e32 vcc, 0, v17
	s_nop 1
	v_cndmask_b32_e32 v57, v242, v57, vcc
	v_cmp_eq_u32_e32 vcc, 0, v66
	s_nop 1
	v_cndmask_b32_e32 v41, v242, v41, vcc
	v_cmp_eq_u32_e32 vcc, 0, v67
	s_nop 1
	v_cndmask_b32_e32 v58, v242, v58, vcc
	v_cmp_eq_u32_e32 vcc, 0, v68
	s_nop 1
	v_cndmask_b32_e32 v42, v242, v42, vcc
	v_cmp_eq_u32_e32 vcc, 0, v69
	s_nop 1
	v_cndmask_b32_e32 v59, v242, v59, vcc
	v_cmp_eq_u32_e32 vcc, 0, v70
	s_nop 1
	v_cndmask_b32_e32 v43, v242, v43, vcc
	v_cmp_eq_u32_e32 vcc, 0, v71
	s_nop 1
	v_cndmask_b32_e32 v60, v242, v60, vcc
	v_cmp_eq_u32_e32 vcc, 0, v72
	s_nop 1
	v_cndmask_b32_e32 v44, v242, v44, vcc
	v_cmp_eq_u32_e32 vcc, 0, v73
	s_nop 1
	v_cndmask_b32_e32 v61, v242, v61, vcc
	v_cmp_eq_u32_e32 vcc, 0, v74
	s_nop 1
	v_cndmask_b32_e32 v45, v242, v45, vcc
	v_cmp_eq_u32_e32 vcc, 0, v75
	s_nop 1
	v_cndmask_b32_e32 v62, v242, v62, vcc
	v_cmp_eq_u32_e32 vcc, 0, v76
	s_nop 1
	v_cndmask_b32_e32 v46, v242, v46, vcc
	v_cmp_eq_u32_e32 vcc, 0, v77
	s_nop 1
	v_cndmask_b32_e32 v63, v242, v63, vcc
	v_cmp_eq_u32_e32 vcc, 0, v4
	v_and_b32_e32 v4, 0x4000000, v3
	v_and_b32_e32 v3, 0x8000000, v3
	v_cndmask_b32_e32 v47, v242, v47, vcc
	v_cmp_eq_u32_e32 vcc, 0, v4
	v_and_b32_e32 v4, 0x4000000, v6
	s_nop 0
	v_cndmask_b32_e32 v64, v242, v64, vcc
	v_cmp_eq_u32_e32 vcc, 0, v4
	s_nop 1
	v_cndmask_b32_e32 v48, v242, v48, vcc
	v_cmp_eq_u32_e32 vcc, 0, v3
	v_and_b32_e32 v3, 0x8000000, v6
	s_nop 0
	v_cndmask_b32_e32 v65, v242, v65, vcc
	v_cmp_eq_u32_e32 vcc, 0, v3
	s_nop 1
	v_cndmask_b32_e32 v49, v242, v49, vcc
